# speedup vs baseline: 1.0156x; 1.0018x over previous
.LBB3_25:
	s_add_i32 s12, s45, s28
	s_add_i32 s2, s43, s40
	s_add_i32 s3, s12, -2
	s_cmp_lt_i32 s3, 0
	s_mov_b32 s3, m0
	s_mov_b32 m0, s2
	s_nop 0
	global_load_lds_dwordx4 v[222:223], off
	s_mov_b32 m0, s3
	s_cbranch_scc1 .LBB3_27
	s_add_i32 s48, s12, -2
	s_lshl_b32 s49, s48, 1
	s_sub_i32 s49, s35, s49
	s_cmp_ge_i32 s49, 2
	s_cbranch_scc1 .LBB3_27
	s_cmp_lt_i32 s49, 0
	s_cbranch_scc1 .Lmfill_a
	s_cmp_eq_u32 s49, 1
	s_cbranch_scc1 .Lmd1_a
	v_sub_u32_e32 v78, v219, v243
	v_cmp_lt_i32_e32 vcc, 0xffffff85, v78
	s_nop 1
	v_cndmask_b32_e32 v115, v241, v115, vcc
	v_cmp_le_i32_e32 vcc, 0xffffff85, v78
	s_nop 1
	v_cndmask_b32_e32 v114, v241, v114, vcc
	v_cmp_le_i32_e32 vcc, 0xffffff87, v78
	s_nop 1
	v_cndmask_b32_e32 v116, v241, v116, vcc
	v_cmp_le_i32_e32 vcc, 0xffffff88, v78
	s_nop 1
	v_cndmask_b32_e32 v117, v241, v117, vcc
	v_cmp_le_i32_e32 vcc, 0xffffff8d, v78
	s_nop 1
	v_cndmask_b32_e32 v118, v241, v118, vcc
	v_cmp_le_i32_e32 vcc, 0xffffff8e, v78
	s_nop 1
	v_cndmask_b32_e32 v119, v241, v119, vcc
	v_cmp_le_i32_e32 vcc, 0xffffff8f, v78
	s_nop 1
	v_cndmask_b32_e32 v120, v241, v120, vcc
	v_cmp_le_i32_e32 vcc, 0xffffff90, v78
	s_nop 1
	v_cndmask_b32_e32 v121, v241, v121, vcc
	v_cmp_le_i32_e32 vcc, 0xffffff95, v78
	s_nop 1
	v_cndmask_b32_e32 v122, v241, v122, vcc
	v_cmp_le_i32_e32 vcc, 0xffffff96, v78
	s_nop 1
	v_cndmask_b32_e32 v123, v241, v123, vcc
	v_cmp_le_i32_e32 vcc, 0xffffff97, v78
	s_nop 1
	v_cndmask_b32_e32 v124, v241, v124, vcc
	v_cmp_le_i32_e32 vcc, 0xffffff98, v78
	s_nop 1
	v_cndmask_b32_e32 v125, v241, v125, vcc
	v_cmp_le_i32_e32 vcc, 0xffffff9d, v78
	s_nop 1
	v_cndmask_b32_e32 v126, v241, v126, vcc
	v_cmp_le_i32_e32 vcc, 0xffffff9e, v78
	s_nop 1
	v_cndmask_b32_e32 v127, v241, v127, vcc
	v_cmp_le_i32_e32 vcc, 0xffffff9f, v78
	s_nop 1
	v_cndmask_b32_e32 v128, v241, v128, vcc
	v_cmp_le_i32_e32 vcc, 0xffffffa0, v78
	s_nop 1
	v_cndmask_b32_e32 v129, v241, v129, vcc
	v_mov_b32_e32 v98, v241
	v_mov_b32_e32 v99, v241
	v_mov_b32_e32 v100, v241
	v_mov_b32_e32 v101, v241
	v_mov_b32_e32 v102, v241
	v_mov_b32_e32 v103, v241
	v_mov_b32_e32 v104, v241
	v_mov_b32_e32 v105, v241
	v_mov_b32_e32 v106, v241
	v_mov_b32_e32 v107, v241
	v_mov_b32_e32 v108, v241
	v_mov_b32_e32 v109, v241
	v_mov_b32_e32 v110, v241
	v_mov_b32_e32 v111, v241
	v_mov_b32_e32 v112, v241
	v_mov_b32_e32 v113, v241
	s_branch .LBB3_27
.Lmd1_a:
	v_sub_u32_e32 v78, v219, v243
	v_cmp_le_i32_e32 vcc, 0xffffffa5, v78
	s_nop 1
	v_cndmask_b32_e32 v98, v241, v98, vcc
	v_cmp_le_i32_e32 vcc, 0xffffffa6, v78
	s_nop 1
	v_cndmask_b32_e32 v99, v241, v99, vcc
	v_cmp_le_i32_e32 vcc, 0xffffffa7, v78
	s_nop 1
	v_cndmask_b32_e32 v100, v241, v100, vcc
	v_cmp_le_i32_e32 vcc, 0xffffffa8, v78
	s_nop 1
	v_cndmask_b32_e32 v101, v241, v101, vcc
	v_cmp_le_i32_e32 vcc, 0xffffffad, v78
	s_nop 1
	v_cndmask_b32_e32 v102, v241, v102, vcc
	v_cmp_le_i32_e32 vcc, 0xffffffae, v78
	s_nop 1
	v_cndmask_b32_e32 v103, v241, v103, vcc
	v_cmp_le_i32_e32 vcc, 0xffffffaf, v78
	s_nop 1
	v_cndmask_b32_e32 v104, v241, v104, vcc
	v_cmp_le_i32_e32 vcc, 0xffffffb0, v78
	s_nop 1
	v_cndmask_b32_e32 v105, v241, v105, vcc
	v_cmp_le_i32_e32 vcc, 0xffffffb5, v78
	s_nop 1
	v_cndmask_b32_e32 v106, v241, v106, vcc
	v_cmp_le_i32_e32 vcc, 0xffffffb6, v78
	s_nop 1
	v_cndmask_b32_e32 v107, v241, v107, vcc
	v_cmp_le_i32_e32 vcc, 0xffffffb7, v78
	s_nop 1
	v_cndmask_b32_e32 v108, v241, v108, vcc
	v_cmp_le_i32_e32 vcc, 0xffffffb8, v78
	s_nop 1
	v_cndmask_b32_e32 v109, v241, v109, vcc
	v_cmp_le_i32_e32 vcc, 0xffffffbd, v78
	s_nop 1
	v_cndmask_b32_e32 v110, v241, v110, vcc
	v_cmp_le_i32_e32 vcc, 0xffffffbe, v78
	s_nop 1
	v_cndmask_b32_e32 v111, v241, v111, vcc
	v_cmp_le_i32_e32 vcc, 0xffffffbf, v78
	s_nop 1
	v_cndmask_b32_e32 v112, v241, v112, vcc
	v_cmp_le_i32_e32 vcc, 0xffffffc0, v78
	s_nop 1
	v_cndmask_b32_e32 v113, v241, v113, vcc
	s_branch .LBB3_27

.LBB3_36:
	s_add_i32 s12, s12, -1
	s_cmp_lt_i32 s12, 0
	s_cbranch_scc1 .LBB3_38
	s_mov_b32 s48, s12
	s_lshl_b32 s49, s48, 1
	s_sub_i32 s49, s35, s49
	s_cmp_ge_i32 s49, 2
	s_cbranch_scc1 .LBB3_38
	s_cmp_lt_i32 s49, 0
	s_cbranch_scc1 .Lmfill_b
	s_cmp_eq_u32 s49, 1
	s_cbranch_scc1 .Lmd1_b
	v_sub_u32_e32 v107, v219, v243
	v_cmp_lt_i32_e32 vcc, 0xffffffc5, v107
	s_nop 1
	v_cndmask_b32_e32 v83, v241, v83, vcc
	v_cmp_le_i32_e32 vcc, 0xffffffc5, v107
	s_nop 1
	v_cndmask_b32_e32 v82, v241, v82, vcc
	v_cmp_le_i32_e32 vcc, 0xffffffc7, v107
	s_nop 1
	v_cndmask_b32_e32 v84, v241, v84, vcc
	v_cmp_le_i32_e32 vcc, 0xffffffc8, v107
	s_nop 1
	v_cndmask_b32_e32 v85, v241, v85, vcc
	v_cmp_le_i32_e32 vcc, 0xffffffcd, v107
	s_nop 1
	v_cndmask_b32_e32 v86, v241, v86, vcc
	v_cmp_le_i32_e32 vcc, 0xffffffce, v107
	s_nop 1
	v_cndmask_b32_e32 v87, v241, v87, vcc
	v_cmp_le_i32_e32 vcc, 0xffffffcf, v107
	s_nop 1
	v_cndmask_b32_e32 v88, v241, v88, vcc
	v_cmp_le_i32_e32 vcc, 0xffffffd0, v107
	s_nop 1
	v_cndmask_b32_e32 v89, v241, v89, vcc
	v_cmp_le_i32_e32 vcc, 0xffffffd5, v107
	s_nop 1
	v_cndmask_b32_e32 v90, v241, v90, vcc
	v_cmp_le_i32_e32 vcc, 0xffffffd6, v107
	s_nop 1
	v_cndmask_b32_e32 v91, v241, v91, vcc
	v_cmp_le_i32_e32 vcc, 0xffffffd7, v107
	s_nop 1
	v_cndmask_b32_e32 v92, v241, v92, vcc
	v_cmp_le_i32_e32 vcc, 0xffffffd8, v107
	s_nop 1
	v_cndmask_b32_e32 v93, v241, v93, vcc
	v_cmp_le_i32_e32 vcc, 0xffffffdd, v107
	s_nop 1
	v_cndmask_b32_e32 v94, v241, v94, vcc
	v_cmp_le_i32_e32 vcc, 0xffffffde, v107
	s_nop 1
	v_cndmask_b32_e32 v95, v241, v95, vcc
	v_cmp_le_i32_e32 vcc, 0xffffffdf, v107
	s_nop 1
	v_cndmask_b32_e32 v96, v241, v96, vcc
	v_cmp_le_i32_e32 vcc, 0xffffffe0, v107
	s_nop 1
	v_cndmask_b32_e32 v97, v241, v97, vcc
	v_mov_b32_e32 v66, v241
	v_mov_b32_e32 v67, v241
	v_mov_b32_e32 v68, v241
	v_mov_b32_e32 v69, v241
	v_mov_b32_e32 v70, v241
	v_mov_b32_e32 v71, v241
	v_mov_b32_e32 v72, v241
	v_mov_b32_e32 v73, v241
	v_mov_b32_e32 v74, v241
	v_mov_b32_e32 v75, v241
	v_mov_b32_e32 v76, v241
	v_mov_b32_e32 v77, v241
	v_mov_b32_e32 v78, v241
	v_mov_b32_e32 v79, v241
	v_mov_b32_e32 v80, v241
	v_mov_b32_e32 v81, v241
	s_branch .LBB3_38
.Lmd1_b:
	v_sub_u32_e32 v107, v219, v243
	v_cmp_le_i32_e32 vcc, 0xffffffe5, v107
	s_nop 1
	v_cndmask_b32_e32 v66, v241, v66, vcc
	v_cmp_le_i32_e32 vcc, 0xffffffe6, v107
	s_nop 1
	v_cndmask_b32_e32 v67, v241, v67, vcc
	v_cmp_le_i32_e32 vcc, 0xffffffe7, v107
	s_nop 1
	v_cndmask_b32_e32 v68, v241, v68, vcc
	v_cmp_le_i32_e32 vcc, 0xffffffe8, v107
	s_nop 1
	v_cndmask_b32_e32 v69, v241, v69, vcc
	v_cmp_le_i32_e32 vcc, 0xffffffed, v107
	s_nop 1
	v_cndmask_b32_e32 v70, v241, v70, vcc
	v_cmp_le_i32_e32 vcc, 0xffffffee, v107
	s_nop 1
	v_cndmask_b32_e32 v71, v241, v71, vcc
	v_cmp_le_i32_e32 vcc, 0xffffffef, v107
	s_nop 1
	v_cndmask_b32_e32 v72, v241, v72, vcc
	v_cmp_le_i32_e32 vcc, -16, v107
	s_nop 1
	v_cndmask_b32_e32 v73, v241, v73, vcc
	v_cmp_le_i32_e32 vcc, -11, v107
	s_nop 1
	v_cndmask_b32_e32 v74, v241, v74, vcc
	v_cmp_le_i32_e32 vcc, -10, v107
	s_nop 1
	v_cndmask_b32_e32 v75, v241, v75, vcc
	v_cmp_le_i32_e32 vcc, -9, v107
	s_nop 1
	v_cndmask_b32_e32 v76, v241, v76, vcc
	v_cmp_le_i32_e32 vcc, -8, v107
	s_nop 1
	v_cndmask_b32_e32 v77, v241, v77, vcc
	v_cmp_le_i32_e32 vcc, -3, v107
	s_nop 1
	v_cndmask_b32_e32 v78, v241, v78, vcc
	v_cmp_le_i32_e32 vcc, -2, v107
	s_nop 1
	v_cndmask_b32_e32 v79, v241, v79, vcc
	v_cmp_le_i32_e32 vcc, -1, v107
	s_nop 1
	v_cndmask_b32_e32 v80, v241, v80, vcc
	v_cmp_le_i32_e32 vcc, 0, v107
	s_nop 1
	v_cndmask_b32_e32 v81, v241, v81, vcc
	s_branch .LBB3_38
